# phase 5 order split by bid bit 0 (whole XCDs run lru_pass2 first or last) instead of bit 3
# speedup vs baseline: 1.0207x; 1.0016x over previous
; #define SEAM(k) do { if (rep_ == REP(k) && IN((k) + 1)) xcd_barrier(bar); } while (0)
; __global__ void __launch_bounds__(NTHREADS, 2) fwd_kernel(Params p) {
;     ...
;     if (IN(5)) for (int rep_ = 0; rep_ <= REP(5); ++rep_) { if (rep_) __syncthreads(); if (!(p.flags & 2)) phase_attn0(p, lds, G, bid); __syncthreads(); if (!(p.flags & 4)) lru_pass2(p, lds, G, bid); SEAM(5); }
.LBB0_530:
	s_cmp_gt_i32 s24, 5
	s_cselect_b64 s[0:1], -1, 0
	s_cmp_lt_i32 s25, 6
	s_cselect_b64 s[2:3], -1, 0
	s_or_b64 s[0:1], s[0:1], s[2:3]
	s_and_b64 vcc, exec, s[0:1]
	s_cbranch_vccnz .LBB0_622
	s_mov_b32 s97, 0
	s_and_b32 s0, s26, 6
	s_cmp_lg_u32 s0, 0
	s_cbranch_scc1 .Lp5_normal
	s_bitcmp1_b32 s22, 0
	s_cbranch_scc0 .Lp5_normal
	s_mov_b32 s97, 1
	s_branch .LBB0_560
